# baseline (speedup 1.0000x reference)
.LBB0_120:
	s_or_b64 exec, exec, s[4:5]
	v_lshrrev_b32_e32 v1, 6, v0
	v_and_b32_e32 v2, 63, v0
	v_mad_u32_u24 v3, v1, 7, v2
	v_cmp_gt_u32_e32 vcc, 7, v2
	v_cmp_gt_u32_e64 s[4:5], 2, v1
	s_and_b64 s[4:5], s[4:5], vcc
	v_mov_b32_e32 v4, 0xff
	v_cndmask_b32_e64 v3, v4, v3, s[4:5]
	v_lshl_add_u32 v5, v2, 1, 14
	v_cmp_gt_u32_e32 vcc, 2, v2
	v_cmp_eq_u32_e64 s[4:5], 2, v1
	s_and_b64 s[4:5], s[4:5], vcc
	s_nop 1
	v_cndmask_b32_e64 v3, v3, v5, s[4:5]
	v_cmp_eq_u32_e32 vcc, 0xc0, v0
	v_mov_b32_e32 v5, 15
	s_nop 1
	v_cndmask_b32_e32 v0, v3, v5, vcc
	s_cmpk_lt_i32 s2, 0x100
	s_cselect_b64 s[4:5], -1, 0
	v_cmp_gt_u32_e32 vcc, 17, v0
	s_and_b64 s[4:5], s[4:5], vcc
	s_waitcnt lgkmcnt(0)
	s_barrier
	s_and_saveexec_b64 s[6:7], s[4:5]
	s_cbranch_execz .LBB0_151
	v_cmp_lt_u32_e32 vcc, 6, v0
	s_and_saveexec_b64 s[4:5], vcc
	s_xor_b64 s[4:5], exec, s[4:5]
	s_cbranch_execz .LBB0_142
	v_cmp_lt_u32_e32 vcc, 13, v0
	s_and_saveexec_b64 s[6:7], vcc
	s_xor_b64 s[6:7], exec, s[6:7]
	s_cbranch_execz .LBB0_138
	v_mov_b32_e32 v1, 0
	ds_read_b32 v1, v1 offset:64
	s_and_b32 s3, s2, 7
	s_ashr_i32 s14, s2, 3
	v_cmp_lt_i32_e32 vcc, 14, v0
	s_mov_b64 s[10:11], 0
	s_waitcnt lgkmcnt(0)
	v_readfirstlane_b32 s15, v1
	s_and_saveexec_b64 s[8:9], vcc
	s_xor_b64 s[8:9], exec, s[8:9]
	s_cbranch_execz .LBB0_133
	v_cmp_eq_u32_e32 vcc, 15, v0
	s_mov_b64 s[12:13], 0
	s_and_saveexec_b64 s[10:11], vcc
	s_cbranch_execz .LBB0_132
	s_cmp_gt_i32 s15, 64
	s_cbranch_scc0 .LBB0_130
	s_cmp_gt_i32 s15, 0x44
	s_cbranch_scc1 .Lxs_p8
	s_lshl_b32 s12, s15, 6
	s_addk_i32 s12, 0xf000
	s_cmp_lt_i32 s2, s12
	s_cbranch_scc0 .LBB0_129
	s_and_b32 s12, s2, 15
	s_mul_i32 s12, s12, 22
	s_lshr_b32 s19, s12, 4
	s_add_i32 s12, s12, 22
	s_lshr_b32 s18, s12, 4
	s_lshl_b32 s12, s2, 16
	s_ashr_i32 s16, s2, 4
	s_addk_i32 s16, 0x100
	s_add_i32 s17, s12, 0x10000
	s_mov_b64 s[12:13], -1
	s_branch .LBB0_131
.Lxs_p8:
	s_lshl_b32 s12, s15, 5
	s_addk_i32 s12, 0xf800
	s_cmp_lt_i32 s2, s12
	s_cbranch_scc0 .LBB0_129
	s_mul_i32 s12, s3, 22
	s_lshr_b32 s19, s12, 3
	s_add_i32 s12, s12, 22
	s_lshr_b32 s18, s12, 3
	s_lshl_b32 s12, s2, 16
	s_add_i32 s16, s14, 0x100
	s_add_i32 s17, s12, 0x10000
	s_mov_b64 s[12:13], -1
	s_branch .LBB0_131

_Z9k_combinePKDF16_PK15HIP_vector_typeIiLj2EEPKS1_IfLj2EEPf:
	s_load_dwordx4 s[4:7], s[0:1], 0x0
	s_load_dwordx4 s[8:11], s[0:1], 0x10
	v_readfirstlane_b32 s12, v0
	v_and_b32_e32 v1, 0x7f, v0
	s_lshl_b32 s13, s2, 1
	v_lshlrev_b32_e32 v2, 4, v1
	v_lshlrev_b32_e32 v3, 5, v1
	s_lshr_b32 s12, s12, 7
	s_or_b32 s12, s13, s12
	s_lshl_b32 s13, s12, 3
	s_lshl_b32 s22, s12, 12
	s_waitcnt lgkmcnt(0)
	s_load_dwordx2 s[14:15], s[6:7], s13
	s_load_dwordx2 s[16:17], s[8:9], s13
	v_lshrrev_b32_e32 v4, 5, v1
	v_and_b32_e32 v5, 31, v1
	v_lshlrev_b32_e32 v7, 21, v4
	v_lshlrev_b32_e32 v4, 20, v4
	v_lshl_or_b32 v4, v5, 4, v4
	v_lshl_or_b32 v7, v5, 4, v7
	s_add_u32 s10, s10, s22
	s_addc_u32 s11, s11, 0
	s_waitcnt lgkmcnt(0)
	s_lshr_b32 s18, s14, 8
	s_lshr_b32 s19, s15, 8
	s_cmp_gt_u32 s18, 63
	s_cbranch_scc1 .Lcmb_a
	s_lshl_b32 s20, s14, 11
	s_add_u32 s20, s4, s20
	s_addc_u32 s21, s5, 0
	global_load_dwordx4 v[8:11], v2, s[20:21]

.Lcmb_slab0:
	s_sub_u32 s22, s4, 0xfffc0
	s_subb_u32 s23, s5, 0
	s_load_dword s24, s[22:23], 0x0
	s_sub_u32 s20, s18, 64
	s_and_b32 s22, s14, 0xff
	s_lshl_b32 s22, s22, 9
	s_waitcnt lgkmcnt(0)
	s_cmp_gt_i32 s24, 0x44
	s_cbranch_scc1 .Lcmb_s8_0
	s_lshl_b32 s20, s20, 23
	s_add_u32 s20, s20, s22
	s_add_u32 s20, s20, 0x2400000
	s_add_u32 s20, s4, s20
	s_addc_u32 s21, s5, 0
	global_load_dwordx4 v[16:19], v7, s[20:21]
	s_add_u32 s20, s20, 0x20000
	s_addc_u32 s21, s21, 0
	global_load_dwordx4 v[20:23], v7, s[20:21]
	s_add_u32 s20, s20, 0x20000
	s_addc_u32 s21, s21, 0
	global_load_dwordx4 v[24:27], v7, s[20:21]
	s_add_u32 s20, s20, 0x20000
	s_addc_u32 s21, s21, 0
	global_load_dwordx4 v[28:31], v7, s[20:21]
	s_add_u32 s20, s20, 0x20000
	s_addc_u32 s21, s21, 0
	global_load_dwordx4 v[32:35], v7, s[20:21]
	s_add_u32 s20, s20, 0x20000
	s_addc_u32 s21, s21, 0
	global_load_dwordx4 v[36:39], v7, s[20:21]
	s_add_u32 s20, s20, 0x20000
	s_addc_u32 s21, s21, 0
	global_load_dwordx4 v[40:43], v7, s[20:21]
	s_add_u32 s20, s20, 0x20000
	s_addc_u32 s21, s21, 0
	global_load_dwordx4 v[44:47], v7, s[20:21]
	s_waitcnt vmcnt(0)
	v_cvt_f32_f16_e32 v48, v16
	v_cvt_f32_f16_sdwa v49, v16 dst_sel:DWORD dst_unused:UNUSED_PAD src0_sel:WORD_1
	v_cvt_f32_f16_e32 v50, v17
	v_cvt_f32_f16_sdwa v51, v17 dst_sel:DWORD dst_unused:UNUSED_PAD src0_sel:WORD_1
	v_cvt_f32_f16_e32 v52, v18
	v_cvt_f32_f16_sdwa v53, v18 dst_sel:DWORD dst_unused:UNUSED_PAD src0_sel:WORD_1
	v_cvt_f32_f16_e32 v54, v19
	v_cvt_f32_f16_sdwa v55, v19 dst_sel:DWORD dst_unused:UNUSED_PAD src0_sel:WORD_1
	v_cvt_f32_f16_e32 v5, v20
	v_cvt_f32_f16_sdwa v6, v20 dst_sel:DWORD dst_unused:UNUSED_PAD src0_sel:WORD_1
	v_add_f32_e32 v48, v48, v5
	v_add_f32_e32 v49, v49, v6
	v_cvt_f32_f16_e32 v5, v21
	v_cvt_f32_f16_sdwa v6, v21 dst_sel:DWORD dst_unused:UNUSED_PAD src0_sel:WORD_1
	v_add_f32_e32 v50, v50, v5
	v_add_f32_e32 v51, v51, v6
	v_cvt_f32_f16_e32 v5, v22
	v_cvt_f32_f16_sdwa v6, v22 dst_sel:DWORD dst_unused:UNUSED_PAD src0_sel:WORD_1
	v_add_f32_e32 v52, v52, v5
	v_add_f32_e32 v53, v53, v6
	v_cvt_f32_f16_e32 v5, v23
	v_cvt_f32_f16_sdwa v6, v23 dst_sel:DWORD dst_unused:UNUSED_PAD src0_sel:WORD_1
	v_add_f32_e32 v54, v54, v5
	v_add_f32_e32 v55, v55, v6
	v_cvt_f32_f16_e32 v5, v24
	v_cvt_f32_f16_sdwa v6, v24 dst_sel:DWORD dst_unused:UNUSED_PAD src0_sel:WORD_1
	v_add_f32_e32 v48, v48, v5
	v_add_f32_e32 v49, v49, v6
	v_cvt_f32_f16_e32 v5, v25
	v_cvt_f32_f16_sdwa v6, v25 dst_sel:DWORD dst_unused:UNUSED_PAD src0_sel:WORD_1
	v_add_f32_e32 v50, v50, v5
	v_add_f32_e32 v51, v51, v6
	v_cvt_f32_f16_e32 v5, v26
	v_cvt_f32_f16_sdwa v6, v26 dst_sel:DWORD dst_unused:UNUSED_PAD src0_sel:WORD_1
	v_add_f32_e32 v52, v52, v5
	v_add_f32_e32 v53, v53, v6
	v_cvt_f32_f16_e32 v5, v27
	v_cvt_f32_f16_sdwa v6, v27 dst_sel:DWORD dst_unused:UNUSED_PAD src0_sel:WORD_1
	v_add_f32_e32 v54, v54, v5
	v_add_f32_e32 v55, v55, v6
	v_cvt_f32_f16_e32 v5, v28
	v_cvt_f32_f16_sdwa v6, v28 dst_sel:DWORD dst_unused:UNUSED_PAD src0_sel:WORD_1
	v_add_f32_e32 v48, v48, v5
	v_add_f32_e32 v49, v49, v6
	v_cvt_f32_f16_e32 v5, v29
	v_cvt_f32_f16_sdwa v6, v29 dst_sel:DWORD dst_unused:UNUSED_PAD src0_sel:WORD_1
	v_add_f32_e32 v50, v50, v5
	v_add_f32_e32 v51, v51, v6
	v_cvt_f32_f16_e32 v5, v30
	v_cvt_f32_f16_sdwa v6, v30 dst_sel:DWORD dst_unused:UNUSED_PAD src0_sel:WORD_1
	v_add_f32_e32 v52, v52, v5
	v_add_f32_e32 v53, v53, v6
	v_cvt_f32_f16_e32 v5, v31
	v_cvt_f32_f16_sdwa v6, v31 dst_sel:DWORD dst_unused:UNUSED_PAD src0_sel:WORD_1
	v_add_f32_e32 v54, v54, v5
	v_add_f32_e32 v55, v55, v6
	v_cvt_f32_f16_e32 v5, v32
	v_cvt_f32_f16_sdwa v6, v32 dst_sel:DWORD dst_unused:UNUSED_PAD src0_sel:WORD_1
	v_add_f32_e32 v48, v48, v5
	v_add_f32_e32 v49, v49, v6
	v_cvt_f32_f16_e32 v5, v33
	v_cvt_f32_f16_sdwa v6, v33 dst_sel:DWORD dst_unused:UNUSED_PAD src0_sel:WORD_1
	v_add_f32_e32 v50, v50, v5
	v_add_f32_e32 v51, v51, v6
	v_cvt_f32_f16_e32 v5, v34
	v_cvt_f32_f16_sdwa v6, v34 dst_sel:DWORD dst_unused:UNUSED_PAD src0_sel:WORD_1
	v_add_f32_e32 v52, v52, v5
	v_add_f32_e32 v53, v53, v6
	v_cvt_f32_f16_e32 v5, v35
	v_cvt_f32_f16_sdwa v6, v35 dst_sel:DWORD dst_unused:UNUSED_PAD src0_sel:WORD_1
	v_add_f32_e32 v54, v54, v5
	v_add_f32_e32 v55, v55, v6
	v_cvt_f32_f16_e32 v5, v36
	v_cvt_f32_f16_sdwa v6, v36 dst_sel:DWORD dst_unused:UNUSED_PAD src0_sel:WORD_1
	v_add_f32_e32 v48, v48, v5
	v_add_f32_e32 v49, v49, v6
	v_cvt_f32_f16_e32 v5, v37
	v_cvt_f32_f16_sdwa v6, v37 dst_sel:DWORD dst_unused:UNUSED_PAD src0_sel:WORD_1
	v_add_f32_e32 v50, v50, v5
	v_add_f32_e32 v51, v51, v6
	v_cvt_f32_f16_e32 v5, v38
	v_cvt_f32_f16_sdwa v6, v38 dst_sel:DWORD dst_unused:UNUSED_PAD src0_sel:WORD_1
	v_add_f32_e32 v52, v52, v5
	v_add_f32_e32 v53, v53, v6
	v_cvt_f32_f16_e32 v5, v39
	v_cvt_f32_f16_sdwa v6, v39 dst_sel:DWORD dst_unused:UNUSED_PAD src0_sel:WORD_1
	v_add_f32_e32 v54, v54, v5
	v_add_f32_e32 v55, v55, v6
	v_cvt_f32_f16_e32 v5, v40
	v_cvt_f32_f16_sdwa v6, v40 dst_sel:DWORD dst_unused:UNUSED_PAD src0_sel:WORD_1
	v_add_f32_e32 v48, v48, v5
	v_add_f32_e32 v49, v49, v6
	v_cvt_f32_f16_e32 v5, v41
	v_cvt_f32_f16_sdwa v6, v41 dst_sel:DWORD dst_unused:UNUSED_PAD src0_sel:WORD_1
	v_add_f32_e32 v50, v50, v5
	v_add_f32_e32 v51, v51, v6
	v_cvt_f32_f16_e32 v5, v42
	v_cvt_f32_f16_sdwa v6, v42 dst_sel:DWORD dst_unused:UNUSED_PAD src0_sel:WORD_1
	v_add_f32_e32 v52, v52, v5
	v_add_f32_e32 v53, v53, v6
	v_cvt_f32_f16_e32 v5, v43
	v_cvt_f32_f16_sdwa v6, v43 dst_sel:DWORD dst_unused:UNUSED_PAD src0_sel:WORD_1
	v_add_f32_e32 v54, v54, v5
	v_add_f32_e32 v55, v55, v6
	v_cvt_f32_f16_e32 v5, v44
	v_cvt_f32_f16_sdwa v6, v44 dst_sel:DWORD dst_unused:UNUSED_PAD src0_sel:WORD_1
	v_add_f32_e32 v48, v48, v5
	v_add_f32_e32 v49, v49, v6
	v_cvt_f32_f16_e32 v5, v45
	v_cvt_f32_f16_sdwa v6, v45 dst_sel:DWORD dst_unused:UNUSED_PAD src0_sel:WORD_1
	v_add_f32_e32 v50, v50, v5
	v_add_f32_e32 v51, v51, v6
	v_cvt_f32_f16_e32 v5, v46
	v_cvt_f32_f16_sdwa v6, v46 dst_sel:DWORD dst_unused:UNUSED_PAD src0_sel:WORD_1
	v_add_f32_e32 v52, v52, v5
	v_add_f32_e32 v53, v53, v6
	v_cvt_f32_f16_e32 v5, v47
	v_cvt_f32_f16_sdwa v6, v47 dst_sel:DWORD dst_unused:UNUSED_PAD src0_sel:WORD_1
	v_add_f32_e32 v54, v54, v5
	v_add_f32_e32 v55, v55, v6
	s_add_u32 s20, s20, 0x20000
	s_addc_u32 s21, s21, 0
	global_load_dwordx4 v[16:19], v7, s[20:21]
	s_add_u32 s20, s20, 0x20000
	s_addc_u32 s21, s21, 0
	global_load_dwordx4 v[20:23], v7, s[20:21]
	s_add_u32 s20, s20, 0x20000
	s_addc_u32 s21, s21, 0
	global_load_dwordx4 v[24:27], v7, s[20:21]
	s_add_u32 s20, s20, 0x20000
	s_addc_u32 s21, s21, 0
	global_load_dwordx4 v[28:31], v7, s[20:21]
	s_add_u32 s20, s20, 0x20000
	s_addc_u32 s21, s21, 0
	global_load_dwordx4 v[32:35], v7, s[20:21]
	s_add_u32 s20, s20, 0x20000
	s_addc_u32 s21, s21, 0
	global_load_dwordx4 v[36:39], v7, s[20:21]
	s_add_u32 s20, s20, 0x20000
	s_addc_u32 s21, s21, 0
	global_load_dwordx4 v[40:43], v7, s[20:21]
	s_add_u32 s20, s20, 0x20000
	s_addc_u32 s21, s21, 0
	global_load_dwordx4 v[44:47], v7, s[20:21]
	s_waitcnt vmcnt(0)
	v_cvt_f32_f16_e32 v5, v16
	v_cvt_f32_f16_sdwa v6, v16 dst_sel:DWORD dst_unused:UNUSED_PAD src0_sel:WORD_1
	v_add_f32_e32 v48, v48, v5
	v_add_f32_e32 v49, v49, v6
	v_cvt_f32_f16_e32 v5, v17
	v_cvt_f32_f16_sdwa v6, v17 dst_sel:DWORD dst_unused:UNUSED_PAD src0_sel:WORD_1
	v_add_f32_e32 v50, v50, v5
	v_add_f32_e32 v51, v51, v6
	v_cvt_f32_f16_e32 v5, v18
	v_cvt_f32_f16_sdwa v6, v18 dst_sel:DWORD dst_unused:UNUSED_PAD src0_sel:WORD_1
	v_add_f32_e32 v52, v52, v5
	v_add_f32_e32 v53, v53, v6
	v_cvt_f32_f16_e32 v5, v19
	v_cvt_f32_f16_sdwa v6, v19 dst_sel:DWORD dst_unused:UNUSED_PAD src0_sel:WORD_1
	v_add_f32_e32 v54, v54, v5
	v_add_f32_e32 v55, v55, v6
	v_cvt_f32_f16_e32 v5, v20
	v_cvt_f32_f16_sdwa v6, v20 dst_sel:DWORD dst_unused:UNUSED_PAD src0_sel:WORD_1
	v_add_f32_e32 v48, v48, v5
	v_add_f32_e32 v49, v49, v6
	v_cvt_f32_f16_e32 v5, v21
	v_cvt_f32_f16_sdwa v6, v21 dst_sel:DWORD dst_unused:UNUSED_PAD src0_sel:WORD_1
	v_add_f32_e32 v50, v50, v5
	v_add_f32_e32 v51, v51, v6
	v_cvt_f32_f16_e32 v5, v22
	v_cvt_f32_f16_sdwa v6, v22 dst_sel:DWORD dst_unused:UNUSED_PAD src0_sel:WORD_1
	v_add_f32_e32 v52, v52, v5
	v_add_f32_e32 v53, v53, v6
	v_cvt_f32_f16_e32 v5, v23
	v_cvt_f32_f16_sdwa v6, v23 dst_sel:DWORD dst_unused:UNUSED_PAD src0_sel:WORD_1
	v_add_f32_e32 v54, v54, v5
	v_add_f32_e32 v55, v55, v6
	v_cvt_f32_f16_e32 v5, v24
	v_cvt_f32_f16_sdwa v6, v24 dst_sel:DWORD dst_unused:UNUSED_PAD src0_sel:WORD_1
	v_add_f32_e32 v48, v48, v5
	v_add_f32_e32 v49, v49, v6
	v_cvt_f32_f16_e32 v5, v25
	v_cvt_f32_f16_sdwa v6, v25 dst_sel:DWORD dst_unused:UNUSED_PAD src0_sel:WORD_1
	v_add_f32_e32 v50, v50, v5
	v_add_f32_e32 v51, v51, v6
	v_cvt_f32_f16_e32 v5, v26
	v_cvt_f32_f16_sdwa v6, v26 dst_sel:DWORD dst_unused:UNUSED_PAD src0_sel:WORD_1
	v_add_f32_e32 v52, v52, v5
	v_add_f32_e32 v53, v53, v6
	v_cvt_f32_f16_e32 v5, v27
	v_cvt_f32_f16_sdwa v6, v27 dst_sel:DWORD dst_unused:UNUSED_PAD src0_sel:WORD_1
	v_add_f32_e32 v54, v54, v5
	v_add_f32_e32 v55, v55, v6
	v_cvt_f32_f16_e32 v5, v28
	v_cvt_f32_f16_sdwa v6, v28 dst_sel:DWORD dst_unused:UNUSED_PAD src0_sel:WORD_1
	v_add_f32_e32 v48, v48, v5
	v_add_f32_e32 v49, v49, v6
	v_cvt_f32_f16_e32 v5, v29
	v_cvt_f32_f16_sdwa v6, v29 dst_sel:DWORD dst_unused:UNUSED_PAD src0_sel:WORD_1
	v_add_f32_e32 v50, v50, v5
	v_add_f32_e32 v51, v51, v6
	v_cvt_f32_f16_e32 v5, v30
	v_cvt_f32_f16_sdwa v6, v30 dst_sel:DWORD dst_unused:UNUSED_PAD src0_sel:WORD_1
	v_add_f32_e32 v52, v52, v5
	v_add_f32_e32 v53, v53, v6
	v_cvt_f32_f16_e32 v5, v31
	v_cvt_f32_f16_sdwa v6, v31 dst_sel:DWORD dst_unused:UNUSED_PAD src0_sel:WORD_1
	v_add_f32_e32 v54, v54, v5
	v_add_f32_e32 v55, v55, v6
	v_cvt_f32_f16_e32 v5, v32
	v_cvt_f32_f16_sdwa v6, v32 dst_sel:DWORD dst_unused:UNUSED_PAD src0_sel:WORD_1
	v_add_f32_e32 v48, v48, v5
	v_add_f32_e32 v49, v49, v6
	v_cvt_f32_f16_e32 v5, v33
	v_cvt_f32_f16_sdwa v6, v33 dst_sel:DWORD dst_unused:UNUSED_PAD src0_sel:WORD_1
	v_add_f32_e32 v50, v50, v5
	v_add_f32_e32 v51, v51, v6
	v_cvt_f32_f16_e32 v5, v34
	v_cvt_f32_f16_sdwa v6, v34 dst_sel:DWORD dst_unused:UNUSED_PAD src0_sel:WORD_1
	v_add_f32_e32 v52, v52, v5
	v_add_f32_e32 v53, v53, v6
	v_cvt_f32_f16_e32 v5, v35
	v_cvt_f32_f16_sdwa v6, v35 dst_sel:DWORD dst_unused:UNUSED_PAD src0_sel:WORD_1
	v_add_f32_e32 v54, v54, v5
	v_add_f32_e32 v55, v55, v6
	v_cvt_f32_f16_e32 v5, v36
	v_cvt_f32_f16_sdwa v6, v36 dst_sel:DWORD dst_unused:UNUSED_PAD src0_sel:WORD_1
	v_add_f32_e32 v48, v48, v5
	v_add_f32_e32 v49, v49, v6
	v_cvt_f32_f16_e32 v5, v37
	v_cvt_f32_f16_sdwa v6, v37 dst_sel:DWORD dst_unused:UNUSED_PAD src0_sel:WORD_1
	v_add_f32_e32 v50, v50, v5
	v_add_f32_e32 v51, v51, v6
	v_cvt_f32_f16_e32 v5, v38
	v_cvt_f32_f16_sdwa v6, v38 dst_sel:DWORD dst_unused:UNUSED_PAD src0_sel:WORD_1
	v_add_f32_e32 v52, v52, v5
	v_add_f32_e32 v53, v53, v6
	v_cvt_f32_f16_e32 v5, v39
	v_cvt_f32_f16_sdwa v6, v39 dst_sel:DWORD dst_unused:UNUSED_PAD src0_sel:WORD_1
	v_add_f32_e32 v54, v54, v5
	v_add_f32_e32 v55, v55, v6
	v_cvt_f32_f16_e32 v5, v40
	v_cvt_f32_f16_sdwa v6, v40 dst_sel:DWORD dst_unused:UNUSED_PAD src0_sel:WORD_1
	v_add_f32_e32 v48, v48, v5
	v_add_f32_e32 v49, v49, v6
	v_cvt_f32_f16_e32 v5, v41
	v_cvt_f32_f16_sdwa v6, v41 dst_sel:DWORD dst_unused:UNUSED_PAD src0_sel:WORD_1
	v_add_f32_e32 v50, v50, v5
	v_add_f32_e32 v51, v51, v6
	v_cvt_f32_f16_e32 v5, v42
	v_cvt_f32_f16_sdwa v6, v42 dst_sel:DWORD dst_unused:UNUSED_PAD src0_sel:WORD_1
	v_add_f32_e32 v52, v52, v5
	v_add_f32_e32 v53, v53, v6
	v_cvt_f32_f16_e32 v5, v43
	v_cvt_f32_f16_sdwa v6, v43 dst_sel:DWORD dst_unused:UNUSED_PAD src0_sel:WORD_1
	v_add_f32_e32 v54, v54, v5
	v_add_f32_e32 v55, v55, v6
	v_cvt_f32_f16_e32 v5, v44
	v_cvt_f32_f16_sdwa v6, v44 dst_sel:DWORD dst_unused:UNUSED_PAD src0_sel:WORD_1
	v_add_f32_e32 v48, v48, v5
	v_add_f32_e32 v49, v49, v6
	v_cvt_f32_f16_e32 v5, v45
	v_cvt_f32_f16_sdwa v6, v45 dst_sel:DWORD dst_unused:UNUSED_PAD src0_sel:WORD_1
	v_add_f32_e32 v50, v50, v5
	v_add_f32_e32 v51, v51, v6
	v_cvt_f32_f16_e32 v5, v46
	v_cvt_f32_f16_sdwa v6, v46 dst_sel:DWORD dst_unused:UNUSED_PAD src0_sel:WORD_1
	v_add_f32_e32 v52, v52, v5
	v_add_f32_e32 v53, v53, v6
	v_cvt_f32_f16_e32 v5, v47
	v_cvt_f32_f16_sdwa v6, v47 dst_sel:DWORD dst_unused:UNUSED_PAD src0_sel:WORD_1
	v_add_f32_e32 v54, v54, v5
	v_add_f32_e32 v55, v55, v6
	s_branch .Lcmb_sd_0
.Lcmb_s8_0:
	s_lshl_b32 s20, s20, 22
	s_add_u32 s20, s20, s22
	s_add_u32 s20, s20, 0x2400000
	s_add_u32 s20, s4, s20
	s_addc_u32 s21, s5, 0
	global_load_dwordx4 v[16:19], v4, s[20:21]
	s_add_u32 s20, s20, 0x20000
	s_addc_u32 s21, s21, 0
	global_load_dwordx4 v[20:23], v4, s[20:21]
	s_add_u32 s20, s20, 0x20000
	s_addc_u32 s21, s21, 0
	global_load_dwordx4 v[24:27], v4, s[20:21]
	s_add_u32 s20, s20, 0x20000
	s_addc_u32 s21, s21, 0
	global_load_dwordx4 v[28:31], v4, s[20:21]
	s_add_u32 s20, s20, 0x20000
	s_addc_u32 s21, s21, 0
	global_load_dwordx4 v[32:35], v4, s[20:21]
	s_add_u32 s20, s20, 0x20000
	s_addc_u32 s21, s21, 0
	global_load_dwordx4 v[36:39], v4, s[20:21]
	s_add_u32 s20, s20, 0x20000
	s_addc_u32 s21, s21, 0
	global_load_dwordx4 v[40:43], v4, s[20:21]
	s_add_u32 s20, s20, 0x20000
	s_addc_u32 s21, s21, 0
	global_load_dwordx4 v[44:47], v4, s[20:21]
	s_waitcnt vmcnt(0)
	v_cvt_f32_f16_e32 v48, v16
	v_cvt_f32_f16_sdwa v49, v16 dst_sel:DWORD dst_unused:UNUSED_PAD src0_sel:WORD_1
	v_cvt_f32_f16_e32 v50, v17
	v_cvt_f32_f16_sdwa v51, v17 dst_sel:DWORD dst_unused:UNUSED_PAD src0_sel:WORD_1
	v_cvt_f32_f16_e32 v52, v18
	v_cvt_f32_f16_sdwa v53, v18 dst_sel:DWORD dst_unused:UNUSED_PAD src0_sel:WORD_1
	v_cvt_f32_f16_e32 v54, v19
	v_cvt_f32_f16_sdwa v55, v19 dst_sel:DWORD dst_unused:UNUSED_PAD src0_sel:WORD_1
	v_cvt_f32_f16_e32 v5, v20
	v_cvt_f32_f16_sdwa v6, v20 dst_sel:DWORD dst_unused:UNUSED_PAD src0_sel:WORD_1
	v_add_f32_e32 v48, v48, v5
	v_add_f32_e32 v49, v49, v6
	v_cvt_f32_f16_e32 v5, v21
	v_cvt_f32_f16_sdwa v6, v21 dst_sel:DWORD dst_unused:UNUSED_PAD src0_sel:WORD_1
	v_add_f32_e32 v50, v50, v5
	v_add_f32_e32 v51, v51, v6
	v_cvt_f32_f16_e32 v5, v22
	v_cvt_f32_f16_sdwa v6, v22 dst_sel:DWORD dst_unused:UNUSED_PAD src0_sel:WORD_1
	v_add_f32_e32 v52, v52, v5
	v_add_f32_e32 v53, v53, v6
	v_cvt_f32_f16_e32 v5, v23
	v_cvt_f32_f16_sdwa v6, v23 dst_sel:DWORD dst_unused:UNUSED_PAD src0_sel:WORD_1
	v_add_f32_e32 v54, v54, v5
	v_add_f32_e32 v55, v55, v6
	v_cvt_f32_f16_e32 v5, v24
	v_cvt_f32_f16_sdwa v6, v24 dst_sel:DWORD dst_unused:UNUSED_PAD src0_sel:WORD_1
	v_add_f32_e32 v48, v48, v5
	v_add_f32_e32 v49, v49, v6
	v_cvt_f32_f16_e32 v5, v25
	v_cvt_f32_f16_sdwa v6, v25 dst_sel:DWORD dst_unused:UNUSED_PAD src0_sel:WORD_1
	v_add_f32_e32 v50, v50, v5
	v_add_f32_e32 v51, v51, v6
	v_cvt_f32_f16_e32 v5, v26
	v_cvt_f32_f16_sdwa v6, v26 dst_sel:DWORD dst_unused:UNUSED_PAD src0_sel:WORD_1
	v_add_f32_e32 v52, v52, v5
	v_add_f32_e32 v53, v53, v6
	v_cvt_f32_f16_e32 v5, v27
	v_cvt_f32_f16_sdwa v6, v27 dst_sel:DWORD dst_unused:UNUSED_PAD src0_sel:WORD_1
	v_add_f32_e32 v54, v54, v5
	v_add_f32_e32 v55, v55, v6
	v_cvt_f32_f16_e32 v5, v28
	v_cvt_f32_f16_sdwa v6, v28 dst_sel:DWORD dst_unused:UNUSED_PAD src0_sel:WORD_1
	v_add_f32_e32 v48, v48, v5
	v_add_f32_e32 v49, v49, v6
	v_cvt_f32_f16_e32 v5, v29
	v_cvt_f32_f16_sdwa v6, v29 dst_sel:DWORD dst_unused:UNUSED_PAD src0_sel:WORD_1
	v_add_f32_e32 v50, v50, v5
	v_add_f32_e32 v51, v51, v6
	v_cvt_f32_f16_e32 v5, v30
	v_cvt_f32_f16_sdwa v6, v30 dst_sel:DWORD dst_unused:UNUSED_PAD src0_sel:WORD_1
	v_add_f32_e32 v52, v52, v5
	v_add_f32_e32 v53, v53, v6
	v_cvt_f32_f16_e32 v5, v31
	v_cvt_f32_f16_sdwa v6, v31 dst_sel:DWORD dst_unused:UNUSED_PAD src0_sel:WORD_1
	v_add_f32_e32 v54, v54, v5
	v_add_f32_e32 v55, v55, v6
	v_cvt_f32_f16_e32 v5, v32
	v_cvt_f32_f16_sdwa v6, v32 dst_sel:DWORD dst_unused:UNUSED_PAD src0_sel:WORD_1
	v_add_f32_e32 v48, v48, v5
	v_add_f32_e32 v49, v49, v6
	v_cvt_f32_f16_e32 v5, v33
	v_cvt_f32_f16_sdwa v6, v33 dst_sel:DWORD dst_unused:UNUSED_PAD src0_sel:WORD_1
	v_add_f32_e32 v50, v50, v5
	v_add_f32_e32 v51, v51, v6
	v_cvt_f32_f16_e32 v5, v34
	v_cvt_f32_f16_sdwa v6, v34 dst_sel:DWORD dst_unused:UNUSED_PAD src0_sel:WORD_1
	v_add_f32_e32 v52, v52, v5
	v_add_f32_e32 v53, v53, v6
	v_cvt_f32_f16_e32 v5, v35
	v_cvt_f32_f16_sdwa v6, v35 dst_sel:DWORD dst_unused:UNUSED_PAD src0_sel:WORD_1
	v_add_f32_e32 v54, v54, v5
	v_add_f32_e32 v55, v55, v6
	v_cvt_f32_f16_e32 v5, v36
	v_cvt_f32_f16_sdwa v6, v36 dst_sel:DWORD dst_unused:UNUSED_PAD src0_sel:WORD_1
	v_add_f32_e32 v48, v48, v5
	v_add_f32_e32 v49, v49, v6
	v_cvt_f32_f16_e32 v5, v37
	v_cvt_f32_f16_sdwa v6, v37 dst_sel:DWORD dst_unused:UNUSED_PAD src0_sel:WORD_1
	v_add_f32_e32 v50, v50, v5
	v_add_f32_e32 v51, v51, v6
	v_cvt_f32_f16_e32 v5, v38
	v_cvt_f32_f16_sdwa v6, v38 dst_sel:DWORD dst_unused:UNUSED_PAD src0_sel:WORD_1
	v_add_f32_e32 v52, v52, v5
	v_add_f32_e32 v53, v53, v6
	v_cvt_f32_f16_e32 v5, v39
	v_cvt_f32_f16_sdwa v6, v39 dst_sel:DWORD dst_unused:UNUSED_PAD src0_sel:WORD_1
	v_add_f32_e32 v54, v54, v5
	v_add_f32_e32 v55, v55, v6
	v_cvt_f32_f16_e32 v5, v40
	v_cvt_f32_f16_sdwa v6, v40 dst_sel:DWORD dst_unused:UNUSED_PAD src0_sel:WORD_1
	v_add_f32_e32 v48, v48, v5
	v_add_f32_e32 v49, v49, v6
	v_cvt_f32_f16_e32 v5, v41
	v_cvt_f32_f16_sdwa v6, v41 dst_sel:DWORD dst_unused:UNUSED_PAD src0_sel:WORD_1
	v_add_f32_e32 v50, v50, v5
	v_add_f32_e32 v51, v51, v6
	v_cvt_f32_f16_e32 v5, v42
	v_cvt_f32_f16_sdwa v6, v42 dst_sel:DWORD dst_unused:UNUSED_PAD src0_sel:WORD_1
	v_add_f32_e32 v52, v52, v5
	v_add_f32_e32 v53, v53, v6
	v_cvt_f32_f16_e32 v5, v43
	v_cvt_f32_f16_sdwa v6, v43 dst_sel:DWORD dst_unused:UNUSED_PAD src0_sel:WORD_1
	v_add_f32_e32 v54, v54, v5
	v_add_f32_e32 v55, v55, v6
	v_cvt_f32_f16_e32 v5, v44
	v_cvt_f32_f16_sdwa v6, v44 dst_sel:DWORD dst_unused:UNUSED_PAD src0_sel:WORD_1
	v_add_f32_e32 v48, v48, v5
	v_add_f32_e32 v49, v49, v6
	v_cvt_f32_f16_e32 v5, v45
	v_cvt_f32_f16_sdwa v6, v45 dst_sel:DWORD dst_unused:UNUSED_PAD src0_sel:WORD_1
	v_add_f32_e32 v50, v50, v5
	v_add_f32_e32 v51, v51, v6
	v_cvt_f32_f16_e32 v5, v46
	v_cvt_f32_f16_sdwa v6, v46 dst_sel:DWORD dst_unused:UNUSED_PAD src0_sel:WORD_1
	v_add_f32_e32 v52, v52, v5
	v_add_f32_e32 v53, v53, v6
	v_cvt_f32_f16_e32 v5, v47
	v_cvt_f32_f16_sdwa v6, v47 dst_sel:DWORD dst_unused:UNUSED_PAD src0_sel:WORD_1
	v_add_f32_e32 v54, v54, v5
	v_add_f32_e32 v55, v55, v6
.Lcmb_sd_0:
.Lcmb_m0:
	v_mul_f32_e32 v56, s16, v48
	v_mul_f32_e32 v57, s16, v49
	v_mul_f32_e32 v58, s16, v50
	v_mul_f32_e32 v59, s16, v51
	v_mul_f32_e32 v60, s16, v52
	v_mul_f32_e32 v61, s16, v53
	v_mul_f32_e32 v62, s16, v54
	v_mul_f32_e32 v63, s16, v55
	s_cmp_gt_u32 s19, 63
	s_cbranch_scc1 .Lcmb_slab1
	v_cvt_f32_f16_e32 v48, v12
	v_cvt_f32_f16_sdwa v49, v12 dst_sel:DWORD dst_unused:UNUSED_PAD src0_sel:WORD_1
	v_cvt_f32_f16_e32 v50, v13
	v_cvt_f32_f16_sdwa v51, v13 dst_sel:DWORD dst_unused:UNUSED_PAD src0_sel:WORD_1
	v_cvt_f32_f16_e32 v52, v14
	v_cvt_f32_f16_sdwa v53, v14 dst_sel:DWORD dst_unused:UNUSED_PAD src0_sel:WORD_1
	v_cvt_f32_f16_e32 v54, v15
	v_cvt_f32_f16_sdwa v55, v15 dst_sel:DWORD dst_unused:UNUSED_PAD src0_sel:WORD_1
	s_branch .Lcmb_m1
.Lcmb_slab1:
	s_sub_u32 s22, s4, 0xfffc0
	s_subb_u32 s23, s5, 0
	s_load_dword s24, s[22:23], 0x0
	s_sub_u32 s20, s19, 64
	s_and_b32 s22, s15, 0xff
	s_lshl_b32 s22, s22, 9
	s_waitcnt lgkmcnt(0)
	s_cmp_gt_i32 s24, 0x44
	s_cbranch_scc1 .Lcmb_s8_1
	s_lshl_b32 s20, s20, 23
	s_add_u32 s20, s20, s22
	s_add_u32 s20, s20, 0x2400000
	s_add_u32 s20, s4, s20
	s_addc_u32 s21, s5, 0
	global_load_dwordx4 v[16:19], v7, s[20:21]
	s_add_u32 s20, s20, 0x20000
	s_addc_u32 s21, s21, 0
	global_load_dwordx4 v[20:23], v7, s[20:21]
	s_add_u32 s20, s20, 0x20000
	s_addc_u32 s21, s21, 0
	global_load_dwordx4 v[24:27], v7, s[20:21]
	s_add_u32 s20, s20, 0x20000
	s_addc_u32 s21, s21, 0
	global_load_dwordx4 v[28:31], v7, s[20:21]
	s_add_u32 s20, s20, 0x20000
	s_addc_u32 s21, s21, 0
	global_load_dwordx4 v[32:35], v7, s[20:21]
	s_add_u32 s20, s20, 0x20000
	s_addc_u32 s21, s21, 0
	global_load_dwordx4 v[36:39], v7, s[20:21]
	s_add_u32 s20, s20, 0x20000
	s_addc_u32 s21, s21, 0
	global_load_dwordx4 v[40:43], v7, s[20:21]
	s_add_u32 s20, s20, 0x20000
	s_addc_u32 s21, s21, 0
	global_load_dwordx4 v[44:47], v7, s[20:21]
	s_waitcnt vmcnt(0)
	v_cvt_f32_f16_e32 v48, v16
	v_cvt_f32_f16_sdwa v49, v16 dst_sel:DWORD dst_unused:UNUSED_PAD src0_sel:WORD_1
	v_cvt_f32_f16_e32 v50, v17
	v_cvt_f32_f16_sdwa v51, v17 dst_sel:DWORD dst_unused:UNUSED_PAD src0_sel:WORD_1
	v_cvt_f32_f16_e32 v52, v18
	v_cvt_f32_f16_sdwa v53, v18 dst_sel:DWORD dst_unused:UNUSED_PAD src0_sel:WORD_1
	v_cvt_f32_f16_e32 v54, v19
	v_cvt_f32_f16_sdwa v55, v19 dst_sel:DWORD dst_unused:UNUSED_PAD src0_sel:WORD_1
	v_cvt_f32_f16_e32 v5, v20
	v_cvt_f32_f16_sdwa v6, v20 dst_sel:DWORD dst_unused:UNUSED_PAD src0_sel:WORD_1
	v_add_f32_e32 v48, v48, v5
	v_add_f32_e32 v49, v49, v6
	v_cvt_f32_f16_e32 v5, v21
	v_cvt_f32_f16_sdwa v6, v21 dst_sel:DWORD dst_unused:UNUSED_PAD src0_sel:WORD_1
	v_add_f32_e32 v50, v50, v5
	v_add_f32_e32 v51, v51, v6
	v_cvt_f32_f16_e32 v5, v22
	v_cvt_f32_f16_sdwa v6, v22 dst_sel:DWORD dst_unused:UNUSED_PAD src0_sel:WORD_1
	v_add_f32_e32 v52, v52, v5
	v_add_f32_e32 v53, v53, v6
	v_cvt_f32_f16_e32 v5, v23
	v_cvt_f32_f16_sdwa v6, v23 dst_sel:DWORD dst_unused:UNUSED_PAD src0_sel:WORD_1
	v_add_f32_e32 v54, v54, v5
	v_add_f32_e32 v55, v55, v6
	v_cvt_f32_f16_e32 v5, v24
	v_cvt_f32_f16_sdwa v6, v24 dst_sel:DWORD dst_unused:UNUSED_PAD src0_sel:WORD_1
	v_add_f32_e32 v48, v48, v5
	v_add_f32_e32 v49, v49, v6
	v_cvt_f32_f16_e32 v5, v25
	v_cvt_f32_f16_sdwa v6, v25 dst_sel:DWORD dst_unused:UNUSED_PAD src0_sel:WORD_1
	v_add_f32_e32 v50, v50, v5
	v_add_f32_e32 v51, v51, v6
	v_cvt_f32_f16_e32 v5, v26
	v_cvt_f32_f16_sdwa v6, v26 dst_sel:DWORD dst_unused:UNUSED_PAD src0_sel:WORD_1
	v_add_f32_e32 v52, v52, v5
	v_add_f32_e32 v53, v53, v6
	v_cvt_f32_f16_e32 v5, v27
	v_cvt_f32_f16_sdwa v6, v27 dst_sel:DWORD dst_unused:UNUSED_PAD src0_sel:WORD_1
	v_add_f32_e32 v54, v54, v5
	v_add_f32_e32 v55, v55, v6
	v_cvt_f32_f16_e32 v5, v28
	v_cvt_f32_f16_sdwa v6, v28 dst_sel:DWORD dst_unused:UNUSED_PAD src0_sel:WORD_1
	v_add_f32_e32 v48, v48, v5
	v_add_f32_e32 v49, v49, v6
	v_cvt_f32_f16_e32 v5, v29
	v_cvt_f32_f16_sdwa v6, v29 dst_sel:DWORD dst_unused:UNUSED_PAD src0_sel:WORD_1
	v_add_f32_e32 v50, v50, v5
	v_add_f32_e32 v51, v51, v6
	v_cvt_f32_f16_e32 v5, v30
	v_cvt_f32_f16_sdwa v6, v30 dst_sel:DWORD dst_unused:UNUSED_PAD src0_sel:WORD_1
	v_add_f32_e32 v52, v52, v5
	v_add_f32_e32 v53, v53, v6
	v_cvt_f32_f16_e32 v5, v31
	v_cvt_f32_f16_sdwa v6, v31 dst_sel:DWORD dst_unused:UNUSED_PAD src0_sel:WORD_1
	v_add_f32_e32 v54, v54, v5
	v_add_f32_e32 v55, v55, v6
	v_cvt_f32_f16_e32 v5, v32
	v_cvt_f32_f16_sdwa v6, v32 dst_sel:DWORD dst_unused:UNUSED_PAD src0_sel:WORD_1
	v_add_f32_e32 v48, v48, v5
	v_add_f32_e32 v49, v49, v6
	v_cvt_f32_f16_e32 v5, v33
	v_cvt_f32_f16_sdwa v6, v33 dst_sel:DWORD dst_unused:UNUSED_PAD src0_sel:WORD_1
	v_add_f32_e32 v50, v50, v5
	v_add_f32_e32 v51, v51, v6
	v_cvt_f32_f16_e32 v5, v34
	v_cvt_f32_f16_sdwa v6, v34 dst_sel:DWORD dst_unused:UNUSED_PAD src0_sel:WORD_1
	v_add_f32_e32 v52, v52, v5
	v_add_f32_e32 v53, v53, v6
	v_cvt_f32_f16_e32 v5, v35
	v_cvt_f32_f16_sdwa v6, v35 dst_sel:DWORD dst_unused:UNUSED_PAD src0_sel:WORD_1
	v_add_f32_e32 v54, v54, v5
	v_add_f32_e32 v55, v55, v6
	v_cvt_f32_f16_e32 v5, v36
	v_cvt_f32_f16_sdwa v6, v36 dst_sel:DWORD dst_unused:UNUSED_PAD src0_sel:WORD_1
	v_add_f32_e32 v48, v48, v5
	v_add_f32_e32 v49, v49, v6
	v_cvt_f32_f16_e32 v5, v37
	v_cvt_f32_f16_sdwa v6, v37 dst_sel:DWORD dst_unused:UNUSED_PAD src0_sel:WORD_1
	v_add_f32_e32 v50, v50, v5
	v_add_f32_e32 v51, v51, v6
	v_cvt_f32_f16_e32 v5, v38
	v_cvt_f32_f16_sdwa v6, v38 dst_sel:DWORD dst_unused:UNUSED_PAD src0_sel:WORD_1
	v_add_f32_e32 v52, v52, v5
	v_add_f32_e32 v53, v53, v6
	v_cvt_f32_f16_e32 v5, v39
	v_cvt_f32_f16_sdwa v6, v39 dst_sel:DWORD dst_unused:UNUSED_PAD src0_sel:WORD_1
	v_add_f32_e32 v54, v54, v5
	v_add_f32_e32 v55, v55, v6
	v_cvt_f32_f16_e32 v5, v40
	v_cvt_f32_f16_sdwa v6, v40 dst_sel:DWORD dst_unused:UNUSED_PAD src0_sel:WORD_1
	v_add_f32_e32 v48, v48, v5
	v_add_f32_e32 v49, v49, v6
	v_cvt_f32_f16_e32 v5, v41
	v_cvt_f32_f16_sdwa v6, v41 dst_sel:DWORD dst_unused:UNUSED_PAD src0_sel:WORD_1
	v_add_f32_e32 v50, v50, v5
	v_add_f32_e32 v51, v51, v6
	v_cvt_f32_f16_e32 v5, v42
	v_cvt_f32_f16_sdwa v6, v42 dst_sel:DWORD dst_unused:UNUSED_PAD src0_sel:WORD_1
	v_add_f32_e32 v52, v52, v5
	v_add_f32_e32 v53, v53, v6
	v_cvt_f32_f16_e32 v5, v43
	v_cvt_f32_f16_sdwa v6, v43 dst_sel:DWORD dst_unused:UNUSED_PAD src0_sel:WORD_1
	v_add_f32_e32 v54, v54, v5
	v_add_f32_e32 v55, v55, v6
	v_cvt_f32_f16_e32 v5, v44
	v_cvt_f32_f16_sdwa v6, v44 dst_sel:DWORD dst_unused:UNUSED_PAD src0_sel:WORD_1
	v_add_f32_e32 v48, v48, v5
	v_add_f32_e32 v49, v49, v6
	v_cvt_f32_f16_e32 v5, v45
	v_cvt_f32_f16_sdwa v6, v45 dst_sel:DWORD dst_unused:UNUSED_PAD src0_sel:WORD_1
	v_add_f32_e32 v50, v50, v5
	v_add_f32_e32 v51, v51, v6
	v_cvt_f32_f16_e32 v5, v46
	v_cvt_f32_f16_sdwa v6, v46 dst_sel:DWORD dst_unused:UNUSED_PAD src0_sel:WORD_1
	v_add_f32_e32 v52, v52, v5
	v_add_f32_e32 v53, v53, v6
	v_cvt_f32_f16_e32 v5, v47
	v_cvt_f32_f16_sdwa v6, v47 dst_sel:DWORD dst_unused:UNUSED_PAD src0_sel:WORD_1
	v_add_f32_e32 v54, v54, v5
	v_add_f32_e32 v55, v55, v6
	s_add_u32 s20, s20, 0x20000
	s_addc_u32 s21, s21, 0
	global_load_dwordx4 v[16:19], v7, s[20:21]
	s_add_u32 s20, s20, 0x20000
	s_addc_u32 s21, s21, 0
	global_load_dwordx4 v[20:23], v7, s[20:21]
	s_add_u32 s20, s20, 0x20000
	s_addc_u32 s21, s21, 0
	global_load_dwordx4 v[24:27], v7, s[20:21]
	s_add_u32 s20, s20, 0x20000
	s_addc_u32 s21, s21, 0
	global_load_dwordx4 v[28:31], v7, s[20:21]
	s_add_u32 s20, s20, 0x20000
	s_addc_u32 s21, s21, 0
	global_load_dwordx4 v[32:35], v7, s[20:21]
	s_add_u32 s20, s20, 0x20000
	s_addc_u32 s21, s21, 0
	global_load_dwordx4 v[36:39], v7, s[20:21]
	s_add_u32 s20, s20, 0x20000
	s_addc_u32 s21, s21, 0
	global_load_dwordx4 v[40:43], v7, s[20:21]
	s_add_u32 s20, s20, 0x20000
	s_addc_u32 s21, s21, 0
	global_load_dwordx4 v[44:47], v7, s[20:21]
	s_waitcnt vmcnt(0)
	v_cvt_f32_f16_e32 v5, v16
	v_cvt_f32_f16_sdwa v6, v16 dst_sel:DWORD dst_unused:UNUSED_PAD src0_sel:WORD_1
	v_add_f32_e32 v48, v48, v5
	v_add_f32_e32 v49, v49, v6
	v_cvt_f32_f16_e32 v5, v17
	v_cvt_f32_f16_sdwa v6, v17 dst_sel:DWORD dst_unused:UNUSED_PAD src0_sel:WORD_1
	v_add_f32_e32 v50, v50, v5
	v_add_f32_e32 v51, v51, v6
	v_cvt_f32_f16_e32 v5, v18
	v_cvt_f32_f16_sdwa v6, v18 dst_sel:DWORD dst_unused:UNUSED_PAD src0_sel:WORD_1
	v_add_f32_e32 v52, v52, v5
	v_add_f32_e32 v53, v53, v6
	v_cvt_f32_f16_e32 v5, v19
	v_cvt_f32_f16_sdwa v6, v19 dst_sel:DWORD dst_unused:UNUSED_PAD src0_sel:WORD_1
	v_add_f32_e32 v54, v54, v5
	v_add_f32_e32 v55, v55, v6
	v_cvt_f32_f16_e32 v5, v20
	v_cvt_f32_f16_sdwa v6, v20 dst_sel:DWORD dst_unused:UNUSED_PAD src0_sel:WORD_1
	v_add_f32_e32 v48, v48, v5
	v_add_f32_e32 v49, v49, v6
	v_cvt_f32_f16_e32 v5, v21
	v_cvt_f32_f16_sdwa v6, v21 dst_sel:DWORD dst_unused:UNUSED_PAD src0_sel:WORD_1
	v_add_f32_e32 v50, v50, v5
	v_add_f32_e32 v51, v51, v6
	v_cvt_f32_f16_e32 v5, v22
	v_cvt_f32_f16_sdwa v6, v22 dst_sel:DWORD dst_unused:UNUSED_PAD src0_sel:WORD_1
	v_add_f32_e32 v52, v52, v5
	v_add_f32_e32 v53, v53, v6
	v_cvt_f32_f16_e32 v5, v23
	v_cvt_f32_f16_sdwa v6, v23 dst_sel:DWORD dst_unused:UNUSED_PAD src0_sel:WORD_1
	v_add_f32_e32 v54, v54, v5
	v_add_f32_e32 v55, v55, v6
	v_cvt_f32_f16_e32 v5, v24
	v_cvt_f32_f16_sdwa v6, v24 dst_sel:DWORD dst_unused:UNUSED_PAD src0_sel:WORD_1
	v_add_f32_e32 v48, v48, v5
	v_add_f32_e32 v49, v49, v6
	v_cvt_f32_f16_e32 v5, v25
	v_cvt_f32_f16_sdwa v6, v25 dst_sel:DWORD dst_unused:UNUSED_PAD src0_sel:WORD_1
	v_add_f32_e32 v50, v50, v5
	v_add_f32_e32 v51, v51, v6
	v_cvt_f32_f16_e32 v5, v26
	v_cvt_f32_f16_sdwa v6, v26 dst_sel:DWORD dst_unused:UNUSED_PAD src0_sel:WORD_1
	v_add_f32_e32 v52, v52, v5
	v_add_f32_e32 v53, v53, v6
	v_cvt_f32_f16_e32 v5, v27
	v_cvt_f32_f16_sdwa v6, v27 dst_sel:DWORD dst_unused:UNUSED_PAD src0_sel:WORD_1
	v_add_f32_e32 v54, v54, v5
	v_add_f32_e32 v55, v55, v6
	v_cvt_f32_f16_e32 v5, v28
	v_cvt_f32_f16_sdwa v6, v28 dst_sel:DWORD dst_unused:UNUSED_PAD src0_sel:WORD_1
	v_add_f32_e32 v48, v48, v5
	v_add_f32_e32 v49, v49, v6
	v_cvt_f32_f16_e32 v5, v29
	v_cvt_f32_f16_sdwa v6, v29 dst_sel:DWORD dst_unused:UNUSED_PAD src0_sel:WORD_1
	v_add_f32_e32 v50, v50, v5
	v_add_f32_e32 v51, v51, v6
	v_cvt_f32_f16_e32 v5, v30
	v_cvt_f32_f16_sdwa v6, v30 dst_sel:DWORD dst_unused:UNUSED_PAD src0_sel:WORD_1
	v_add_f32_e32 v52, v52, v5
	v_add_f32_e32 v53, v53, v6
	v_cvt_f32_f16_e32 v5, v31
	v_cvt_f32_f16_sdwa v6, v31 dst_sel:DWORD dst_unused:UNUSED_PAD src0_sel:WORD_1
	v_add_f32_e32 v54, v54, v5
	v_add_f32_e32 v55, v55, v6
	v_cvt_f32_f16_e32 v5, v32
	v_cvt_f32_f16_sdwa v6, v32 dst_sel:DWORD dst_unused:UNUSED_PAD src0_sel:WORD_1
	v_add_f32_e32 v48, v48, v5
	v_add_f32_e32 v49, v49, v6
	v_cvt_f32_f16_e32 v5, v33
	v_cvt_f32_f16_sdwa v6, v33 dst_sel:DWORD dst_unused:UNUSED_PAD src0_sel:WORD_1
	v_add_f32_e32 v50, v50, v5
	v_add_f32_e32 v51, v51, v6
	v_cvt_f32_f16_e32 v5, v34
	v_cvt_f32_f16_sdwa v6, v34 dst_sel:DWORD dst_unused:UNUSED_PAD src0_sel:WORD_1
	v_add_f32_e32 v52, v52, v5
	v_add_f32_e32 v53, v53, v6
	v_cvt_f32_f16_e32 v5, v35
	v_cvt_f32_f16_sdwa v6, v35 dst_sel:DWORD dst_unused:UNUSED_PAD src0_sel:WORD_1
	v_add_f32_e32 v54, v54, v5
	v_add_f32_e32 v55, v55, v6
	v_cvt_f32_f16_e32 v5, v36
	v_cvt_f32_f16_sdwa v6, v36 dst_sel:DWORD dst_unused:UNUSED_PAD src0_sel:WORD_1
	v_add_f32_e32 v48, v48, v5
	v_add_f32_e32 v49, v49, v6
	v_cvt_f32_f16_e32 v5, v37
	v_cvt_f32_f16_sdwa v6, v37 dst_sel:DWORD dst_unused:UNUSED_PAD src0_sel:WORD_1
	v_add_f32_e32 v50, v50, v5
	v_add_f32_e32 v51, v51, v6
	v_cvt_f32_f16_e32 v5, v38
	v_cvt_f32_f16_sdwa v6, v38 dst_sel:DWORD dst_unused:UNUSED_PAD src0_sel:WORD_1
	v_add_f32_e32 v52, v52, v5
	v_add_f32_e32 v53, v53, v6
	v_cvt_f32_f16_e32 v5, v39
	v_cvt_f32_f16_sdwa v6, v39 dst_sel:DWORD dst_unused:UNUSED_PAD src0_sel:WORD_1
	v_add_f32_e32 v54, v54, v5
	v_add_f32_e32 v55, v55, v6
	v_cvt_f32_f16_e32 v5, v40
	v_cvt_f32_f16_sdwa v6, v40 dst_sel:DWORD dst_unused:UNUSED_PAD src0_sel:WORD_1
	v_add_f32_e32 v48, v48, v5
	v_add_f32_e32 v49, v49, v6
	v_cvt_f32_f16_e32 v5, v41
	v_cvt_f32_f16_sdwa v6, v41 dst_sel:DWORD dst_unused:UNUSED_PAD src0_sel:WORD_1
	v_add_f32_e32 v50, v50, v5
	v_add_f32_e32 v51, v51, v6
	v_cvt_f32_f16_e32 v5, v42
	v_cvt_f32_f16_sdwa v6, v42 dst_sel:DWORD dst_unused:UNUSED_PAD src0_sel:WORD_1
	v_add_f32_e32 v52, v52, v5
	v_add_f32_e32 v53, v53, v6
	v_cvt_f32_f16_e32 v5, v43
	v_cvt_f32_f16_sdwa v6, v43 dst_sel:DWORD dst_unused:UNUSED_PAD src0_sel:WORD_1
	v_add_f32_e32 v54, v54, v5
	v_add_f32_e32 v55, v55, v6
	v_cvt_f32_f16_e32 v5, v44
	v_cvt_f32_f16_sdwa v6, v44 dst_sel:DWORD dst_unused:UNUSED_PAD src0_sel:WORD_1
	v_add_f32_e32 v48, v48, v5
	v_add_f32_e32 v49, v49, v6
	v_cvt_f32_f16_e32 v5, v45
	v_cvt_f32_f16_sdwa v6, v45 dst_sel:DWORD dst_unused:UNUSED_PAD src0_sel:WORD_1
	v_add_f32_e32 v50, v50, v5
	v_add_f32_e32 v51, v51, v6
	v_cvt_f32_f16_e32 v5, v46
	v_cvt_f32_f16_sdwa v6, v46 dst_sel:DWORD dst_unused:UNUSED_PAD src0_sel:WORD_1
	v_add_f32_e32 v52, v52, v5
	v_add_f32_e32 v53, v53, v6
	v_cvt_f32_f16_e32 v5, v47
	v_cvt_f32_f16_sdwa v6, v47 dst_sel:DWORD dst_unused:UNUSED_PAD src0_sel:WORD_1
	v_add_f32_e32 v54, v54, v5
	v_add_f32_e32 v55, v55, v6
	s_branch .Lcmb_sd_1

.Lcmb_sd_1:
.Lcmb_m1:
	v_fmac_f32_e32 v56, s17, v48
	v_fmac_f32_e32 v57, s17, v49
	v_fmac_f32_e32 v58, s17, v50
	v_fmac_f32_e32 v59, s17, v51
	v_fmac_f32_e32 v60, s17, v52
	v_fmac_f32_e32 v61, s17, v53
	v_fmac_f32_e32 v62, s17, v54
	v_fmac_f32_e32 v63, s17, v55
	global_store_dwordx4 v3, v[56:59], s[10:11]
	global_store_dwordx4 v3, v[60:63], s[10:11] offset:16
	s_endpgm
	.p2align	8

	.amdhsa_kernel _Z9k_combinePKDF16_PK15HIP_vector_typeIiLj2EEPKS1_IfLj2EEPf
		.amdhsa_group_segment_fixed_size 0
		.amdhsa_private_segment_fixed_size 0
		.amdhsa_kernarg_size 32
		.amdhsa_user_sgpr_count 2
		.amdhsa_user_sgpr_dispatch_ptr 0
		.amdhsa_user_sgpr_queue_ptr 0
		.amdhsa_user_sgpr_kernarg_segment_ptr 1
		.amdhsa_user_sgpr_dispatch_id 0
		.amdhsa_user_sgpr_kernarg_preload_length 0
		.amdhsa_user_sgpr_kernarg_preload_offset 0
		.amdhsa_user_sgpr_private_segment_size 0
		.amdhsa_uses_dynamic_stack 0
		.amdhsa_enable_private_segment 0
		.amdhsa_system_sgpr_workgroup_id_x 1
		.amdhsa_system_sgpr_workgroup_id_y 0
		.amdhsa_system_sgpr_workgroup_id_z 0
		.amdhsa_system_sgpr_workgroup_info 0
		.amdhsa_system_vgpr_workitem_id 0
		.amdhsa_next_free_vgpr 64
		.amdhsa_next_free_sgpr 26
		.amdhsa_accum_offset 64
		.amdhsa_reserve_vcc 1
		.amdhsa_float_round_mode_32 0
		.amdhsa_float_round_mode_16_64 0
		.amdhsa_float_denorm_mode_32 3
		.amdhsa_float_denorm_mode_16_64 3
		.amdhsa_dx10_clamp 1
		.amdhsa_ieee_mode 1
		.amdhsa_fp16_overflow 0
		.amdhsa_tg_split 0
		.amdhsa_exception_fp_ieee_invalid_op 0
		.amdhsa_exception_fp_denorm_src 0
		.amdhsa_exception_fp_ieee_div_zero 0
		.amdhsa_exception_fp_ieee_overflow 0
		.amdhsa_exception_fp_ieee_underflow 0
		.amdhsa_exception_fp_ieee_inexact 0
		.amdhsa_exception_int_div_zero 0
	.end_amdhsa_kernel

.Lfunc_end3:
	.size	_Z9k_combinePKDF16_PK15HIP_vector_typeIiLj2EEPKS1_IfLj2EEPf, .Lfunc_end3-_Z9k_combinePKDF16_PK15HIP_vector_typeIiLj2EEPKS1_IfLj2EEPf
	.set _Z9k_combinePKDF16_PK15HIP_vector_typeIiLj2EEPKS1_IfLj2EEPf.num_vgpr, 64
	.set _Z9k_combinePKDF16_PK15HIP_vector_typeIiLj2EEPKS1_IfLj2EEPf.num_agpr, 0
	.set _Z9k_combinePKDF16_PK15HIP_vector_typeIiLj2EEPKS1_IfLj2EEPf.numbered_sgpr, 26
	.set _Z9k_combinePKDF16_PK15HIP_vector_typeIiLj2EEPKS1_IfLj2EEPf.num_named_barrier, 0
	.set _Z9k_combinePKDF16_PK15HIP_vector_typeIiLj2EEPKS1_IfLj2EEPf.private_seg_size, 0
	.set _Z9k_combinePKDF16_PK15HIP_vector_typeIiLj2EEPKS1_IfLj2EEPf.uses_vcc, 1
	.set _Z9k_combinePKDF16_PK15HIP_vector_typeIiLj2EEPKS1_IfLj2EEPf.uses_flat_scratch, 0
	.set _Z9k_combinePKDF16_PK15HIP_vector_typeIiLj2EEPKS1_IfLj2EEPf.has_dyn_sized_stack, 0
	.set _Z9k_combinePKDF16_PK15HIP_vector_typeIiLj2EEPKS1_IfLj2EEPf.has_recursion, 0
	.set _Z9k_combinePKDF16_PK15HIP_vector_typeIiLj2EEPKS1_IfLj2EEPf.has_indirect_call, 0

amdhsa.kernels:
  - .agpr_count:     0
    .args:
      - .actual_access:  read_only
        .address_space:  global
        .offset:         0
        .size:           8
        .value_kind:     global_buffer
      - .actual_access:  read_only
        .address_space:  global
        .offset:         8
        .size:           8
        .value_kind:     global_buffer
      - .actual_access:  write_only
        .address_space:  global
        .offset:         16
        .size:           8
        .value_kind:     global_buffer
      - .actual_access:  write_only
        .address_space:  global
        .offset:         24
        .size:           8
        .value_kind:     global_buffer
      - .actual_access:  write_only
        .address_space:  global
        .offset:         32
        .size:           8
        .value_kind:     global_buffer
      - .actual_access:  write_only
        .address_space:  global
        .offset:         40
        .size:           8
        .value_kind:     global_buffer
    .group_segment_fixed_size: 256
    .kernarg_segment_align: 8
    .kernarg_segment_size: 48
    .language:       OpenCL C
    .language_version:
      - 2
      - 0
    .max_flat_workgroup_size: 256
    .name:           _Z10k_xscatterPKiS0_P15HIP_vector_typeIiLj2EEPtP4MetaS3_
    .private_segment_fixed_size: 0
    .sgpr_count:     41
    .sgpr_spill_count: 0
    .symbol:         _Z10k_xscatterPKiS0_P15HIP_vector_typeIiLj2EEPtP4MetaS3_.kd
    .uniform_work_group_size: 1
    .uses_dynamic_stack: false
    .vgpr_count:     55
    .vgpr_spill_count: 0
    .wavefront_size: 64
  - .agpr_count:     0
    .args:
      - .actual_access:  read_only
        .address_space:  global
        .offset:         0
        .size:           8
        .value_kind:     global_buffer
      - .actual_access:  read_only
        .address_space:  global
        .offset:         8
        .size:           8
        .value_kind:     global_buffer
      - .actual_access:  write_only
        .address_space:  global
        .offset:         16
        .size:           8
        .value_kind:     global_buffer
      - .actual_access:  write_only
        .address_space:  global
        .offset:         24
        .size:           8
        .value_kind:     global_buffer
      - .actual_access:  write_only
        .address_space:  global
        .offset:         32
        .size:           8
        .value_kind:     global_buffer
      - .actual_access:  read_only
        .address_space:  global
        .offset:         40
        .size:           8
        .value_kind:     global_buffer
      - .actual_access:  read_only
        .address_space:  global
        .offset:         48
        .size:           8
        .value_kind:     global_buffer
      - .actual_access:  write_only
        .address_space:  global
        .offset:         56
        .size:           8
        .value_kind:     global_buffer
      - .actual_access:  write_only
        .address_space:  global
        .offset:         64
        .size:           8
        .value_kind:     global_buffer
    .group_segment_fixed_size: 4096
    .kernarg_segment_align: 8
    .kernarg_segment_size: 72
    .language:       OpenCL C
    .language_version:
      - 2
      - 0
    .max_flat_workgroup_size: 256
    .name:           _Z5k_prePKfS0_PiP15HIP_vector_typeIfLj2EES1_S0_S0_PDF16_S5_
    .private_segment_fixed_size: 0
    .sgpr_count:     38
    .sgpr_spill_count: 0
    .symbol:         _Z5k_prePKfS0_PiP15HIP_vector_typeIfLj2EES1_S0_S0_PDF16_S5_.kd
    .uniform_work_group_size: 1
    .uses_dynamic_stack: false
    .vgpr_count:     128
    .vgpr_spill_count: 0
    .wavefront_size: 64
  - .agpr_count:     0
    .args:
      - .address_space:  global
        .offset:         0
        .size:           8
        .value_kind:     global_buffer
      - .address_space:  global
        .offset:         8
        .size:           8
        .value_kind:     global_buffer
      - .actual_access:  write_only
        .address_space:  global
        .offset:         16
        .size:           8
        .value_kind:     global_buffer
      - .actual_access:  read_only
        .address_space:  global
        .offset:         24
        .size:           8
        .value_kind:     global_buffer
    .group_segment_fixed_size: 0
    .kernarg_segment_align: 8
    .kernarg_segment_size: 32
    .language:       OpenCL C
    .language_version:
      - 2
      - 0
    .max_flat_workgroup_size: 512
    .name:           _Z7k_gemm2PKDF16_S0_PDF16_PK15HIP_vector_typeIiLj2EE
    .private_segment_fixed_size: 0
    .sgpr_count:     74
    .sgpr_spill_count: 0
    .symbol:         _Z7k_gemm2PKDF16_S0_PDF16_PK15HIP_vector_typeIiLj2EE.kd
    .uniform_work_group_size: 1
    .uses_dynamic_stack: false
    .vgpr_count:     226
    .vgpr_spill_count: 0
    .wavefront_size: 64
  - .agpr_count:     0
    .args:
      - .actual_access:  read_only
        .address_space:  global
        .offset:         0
        .size:           8
        .value_kind:     global_buffer
      - .actual_access:  read_only
        .address_space:  global
        .offset:         8
        .size:           8
        .value_kind:     global_buffer
      - .actual_access:  read_only
        .address_space:  global
        .offset:         16
        .size:           8
        .value_kind:     global_buffer
      - .actual_access:  write_only
        .address_space:  global
        .offset:         24
        .size:           8
        .value_kind:     global_buffer
    .group_segment_fixed_size: 0
    .kernarg_segment_align: 8
    .kernarg_segment_size: 32
    .language:       OpenCL C
    .language_version:
      - 2
      - 0
    .max_flat_workgroup_size: 256
    .name:           _Z9k_combinePKDF16_PK15HIP_vector_typeIiLj2EEPKS1_IfLj2EEPf
    .private_segment_fixed_size: 0
    .sgpr_count:     32
    .sgpr_spill_count: 0
    .symbol:         _Z9k_combinePKDF16_PK15HIP_vector_typeIiLj2EEPKS1_IfLj2EEPf.kd
    .uniform_work_group_size: 1
    .uses_dynamic_stack: false
    .vgpr_count:     64
    .vgpr_spill_count: 0
    .wavefront_size: 64
  - .agpr_count:     0
    .args:
      - .address_space:  global
        .offset:         0
        .size:           8
        .value_kind:     global_buffer
      - .address_space:  global
        .offset:         8
        .size:           8
        .value_kind:     global_buffer
      - .actual_access:  write_only
        .address_space:  global
        .offset:         16
        .size:           8
        .value_kind:     global_buffer
      - .actual_access:  read_only
        .address_space:  global
        .offset:         24
        .size:           8
        .value_kind:     global_buffer
      - .address_space:  global
        .offset:         32
        .size:           8
        .value_kind:     global_buffer
      - .address_space:  global
        .offset:         40
        .size:           8
        .value_kind:     global_buffer
      - .actual_access:  write_only
        .address_space:  global
        .offset:         48
        .size:           8
        .value_kind:     global_buffer
      - .address_space:  global
        .offset:         56
        .size:           8
        .value_kind:     global_buffer
    .group_segment_fixed_size: 0
    .kernarg_segment_align: 8
    .kernarg_segment_size: 64
    .language:       OpenCL C
    .language_version:
      - 2
      - 0
    .max_flat_workgroup_size: 512
    .name:           _Z7k_gemm1ILi0EEvPKDF16_S1_PDF16_PK15HIP_vector_typeIiLj2EEPKfS8_S2_PKt
    .private_segment_fixed_size: 0
    .sgpr_count:     106
    .sgpr_spill_count: 0
    .symbol:         _Z7k_gemm1ILi0EEvPKDF16_S1_PDF16_PK15HIP_vector_typeIiLj2EEPKfS8_S2_PKt.kd
    .uniform_work_group_size: 1
    .uses_dynamic_stack: false
    .vgpr_count:     256
    .vgpr_spill_count: 0
    .wavefront_size: 64
  - .agpr_count:     0
    .args:
      - .address_space:  global
        .offset:         0
        .size:           8
        .value_kind:     global_buffer
      - .address_space:  global
        .offset:         8
        .size:           8
        .value_kind:     global_buffer
      - .actual_access:  write_only
        .address_space:  global
        .offset:         16
        .size:           8
        .value_kind:     global_buffer
      - .actual_access:  read_only
        .address_space:  global
        .offset:         24
        .size:           8
        .value_kind:     global_buffer
      - .address_space:  global
        .offset:         32
        .size:           8
        .value_kind:     global_buffer
      - .actual_access:  read_only
        .address_space:  global
        .offset:         40
        .size:           8
        .value_kind:     global_buffer
      - .actual_access:  write_only
        .address_space:  global
        .offset:         48
        .size:           8
        .value_kind:     global_buffer
      - .address_space:  global
        .offset:         56
        .size:           8
        .value_kind:     global_buffer
    .group_segment_fixed_size: 0
    .kernarg_segment_align: 8
    .kernarg_segment_size: 64
    .language:       OpenCL C
    .language_version:
      - 2
      - 0
    .max_flat_workgroup_size: 512
    .name:           _Z7k_gemm1ILi1EEvPKDF16_S1_PDF16_PK15HIP_vector_typeIiLj2EEPKfS8_S2_PKt
    .private_segment_fixed_size: 0
    .sgpr_count:     96
    .sgpr_spill_count: 0
    .symbol:         _Z7k_gemm1ILi1EEvPKDF16_S1_PDF16_PK15HIP_vector_typeIiLj2EEPKfS8_S2_PKt.kd
    .uniform_work_group_size: 1
    .uses_dynamic_stack: false
    .vgpr_count:     254
    .vgpr_spill_count: 0
    .wavefront_size: 64
